# speedup vs baseline: 1.0105x; 1.0105x over previous
_Z9ssim_mainPKfS0_S0_Pf:
	v_readfirstlane_b32 s29, v0
	s_load_dwordx4 s[4:7], s[0:1], 0x0
	s_load_dwordx4 s[8:11], s[0:1], 0x10
	s_mov_b32 s51, 0x44800000
	s_mov_b32 s38, 0
	s_mov_b32 s39, -1
	s_lshr_b32 s12, s29, 6
	s_mov_b32 s13, s2
	s_lshr_b32 s14, s13, 3
	s_and_b32 s15, s13, 7
	s_lshl_b32 s16, s14, 20
	s_lshl_b32 s17, s15, 17
	s_add_u32 s16, s16, s17
	s_lshl_b32 s17, s12, 8
	s_add_u32 s16, s16, s17
	s_lshl_b32 s27, s12, 2
	s_add_u32 s27, s27, 0x10000
	v_and_b32_e32 v8, 63, v0
	v_and_b32_e32 v169, 15, v0
	v_bfe_u32 v164, v0, 4, 2
	v_lshrrev_b32_e32 v167, 2, v169
	v_lshlrev_b32_e32 v167, 5, v167
	v_and_b32_e32 v168, 1, v169
	v_lshl_or_b32 v167, v168, 4, v167
	v_bfe_u32 v168, v169, 1, 1
	v_lshl_or_b32 v167, v168, 7, v167
	v_lshl_or_b32 v9, v164, 14, v167
	v_and_b32_e32 v168, 1, v164
	v_lshl_or_b32 v23, v168, 14, v167
	v_lshrrev_b32_e32 v168, 1, v164
	v_lshl_or_b32 v23, v168, 13, v23
	v_add_u32_e32 v237, 0x1000, v9
	v_add_u32_e32 v238, 0x2000, v9
	v_add_u32_e32 v239, 0x3000, v9
	v_add_u32_e32 v240, 0x10000, v9
	v_add_u32_e32 v241, 0x11000, v9
	v_add_u32_e32 v242, 0x12000, v9
	v_add_u32_e32 v243, 0x13000, v9
	s_waitcnt lgkmcnt(0)
	s_load_dwordx8 s[40:47], s[8:9], 0x0
	s_load_dwordx2 s[48:49], s[8:9], 0x20
	s_load_dword s50, s[8:9], 0x28
	s_add_u32 s18, s4, s16
	s_addc_u32 s19, s5, 0
	s_add_u32 s20, s6, s16
	s_addc_u32 s21, s7, 0
	global_load_dwordx4 v[36:39], v9, s[18:19] offset:0 sc1 nt
	global_load_dwordx4 v[40:43], v9, s[18:19] offset:2048 sc1 nt
	global_load_dwordx4 v[68:71], v9, s[20:21] offset:0 sc1 nt
	global_load_dwordx4 v[72:75], v9, s[20:21] offset:2048 sc1 nt
	global_load_dwordx4 v[44:47], v237, s[18:19] offset:0 sc1 nt
	global_load_dwordx4 v[48:51], v237, s[18:19] offset:2048 sc1 nt
	global_load_dwordx4 v[76:79], v237, s[20:21] offset:0 sc1 nt
	global_load_dwordx4 v[80:83], v237, s[20:21] offset:2048 sc1 nt
	global_load_dwordx4 v[52:55], v238, s[18:19] offset:0 sc1 nt
	global_load_dwordx4 v[56:59], v238, s[18:19] offset:2048 sc1 nt
	global_load_dwordx4 v[84:87], v238, s[20:21] offset:0 sc1 nt
	global_load_dwordx4 v[88:91], v238, s[20:21] offset:2048 sc1 nt
	global_load_dwordx4 v[60:63], v239, s[18:19] offset:0 sc1 nt
	global_load_dwordx4 v[64:67], v239, s[18:19] offset:2048 sc1 nt
	global_load_dwordx4 v[92:95], v239, s[20:21] offset:0 sc1 nt
	global_load_dwordx4 v[96:99], v239, s[20:21] offset:2048 sc1 nt
	v_mov_b32_e32 v6, s27
	v_mov_b32_e32 v168, 0
	ds_write_b32 v6, v168 offset:0
	ds_write_b32 v6, v168 offset:32
	ds_write_b32 v6, v168 offset:64
	ds_write_b32 v6, v168 offset:96
	v_lshlrev_b32_e32 v167, 3, v164
	v_xor_b32_e32 v168, 16, v167
	v_sub_u32_e32 v165, v167, v169
	v_sub_u32_e32 v166, v168, v169
	v_add_u32_e32 v172, 0, v165
	v_min_u32_e32 v172, 11, v172
	v_lshlrev_b32_e32 v172, 2, v172
	v_add_u32_e32 v173, 1, v165
	v_min_u32_e32 v173, 11, v173
	v_lshlrev_b32_e32 v173, 2, v173
	v_add_u32_e32 v174, 2, v165
	v_min_u32_e32 v174, 11, v174
	v_lshlrev_b32_e32 v174, 2, v174
	v_add_u32_e32 v175, 3, v165
	v_min_u32_e32 v175, 11, v175
	v_lshlrev_b32_e32 v175, 2, v175
	v_add_u32_e32 v176, 4, v165
	v_min_u32_e32 v176, 11, v176
	v_lshlrev_b32_e32 v176, 2, v176
	v_add_u32_e32 v177, 5, v165
	v_min_u32_e32 v177, 11, v177
	v_lshlrev_b32_e32 v177, 2, v177
	v_add_u32_e32 v178, 6, v165
	v_min_u32_e32 v178, 11, v178
	v_lshlrev_b32_e32 v178, 2, v178
	v_add_u32_e32 v179, 7, v165
	v_min_u32_e32 v179, 11, v179
	v_lshlrev_b32_e32 v179, 2, v179
	v_add_u32_e32 v180, 0, v166
	v_min_u32_e32 v180, 11, v180
	v_lshlrev_b32_e32 v180, 2, v180
	v_add_u32_e32 v181, 1, v166
	v_min_u32_e32 v181, 11, v181
	v_lshlrev_b32_e32 v181, 2, v181
	v_add_u32_e32 v182, 2, v166
	v_min_u32_e32 v182, 11, v182
	v_lshlrev_b32_e32 v182, 2, v182
	v_add_u32_e32 v183, 3, v166
	v_min_u32_e32 v183, 11, v183
	v_lshlrev_b32_e32 v183, 2, v183
	v_add_u32_e32 v184, 4, v166
	v_min_u32_e32 v184, 11, v184
	v_lshlrev_b32_e32 v184, 2, v184
	v_add_u32_e32 v185, 5, v166
	v_min_u32_e32 v185, 11, v185
	v_lshlrev_b32_e32 v185, 2, v185
	v_add_u32_e32 v186, 6, v166
	v_min_u32_e32 v186, 11, v186
	v_lshlrev_b32_e32 v186, 2, v186
	v_add_u32_e32 v187, 7, v166
	v_min_u32_e32 v187, 11, v187
	v_lshlrev_b32_e32 v187, 2, v187
	s_cmp_eq_u32 s15, 7
	s_cselect_b32 s22, 0, 0x20000
	s_add_u32 s84, s18, s22
	s_addc_u32 s85, s19, 0
	s_add_u32 s86, s18, s22
	s_addc_u32 s87, s19, 0
	s_add_u32 s86, s86, 0x1000
	s_addc_u32 s87, s87, 0
	s_add_u32 s88, s20, s22
	s_addc_u32 s89, s21, 0
	s_add_u32 s90, s20, s22
	s_addc_u32 s91, s21, 0
	s_add_u32 s90, s90, 0x1000
	s_addc_u32 s91, s91, 0
	s_waitcnt lgkmcnt(0)
	v_writelane_b32 v171, s40, 0
	v_writelane_b32 v171, s41, 1
	v_writelane_b32 v171, s42, 2
	v_writelane_b32 v171, s43, 3
	v_writelane_b32 v171, s44, 4
	v_writelane_b32 v171, s45, 5
	v_writelane_b32 v171, s46, 6
	v_writelane_b32 v171, s47, 7
	v_writelane_b32 v171, s48, 8
	v_writelane_b32 v171, s49, 9
	v_writelane_b32 v171, s50, 10
	v_writelane_b32 v171, 0, 11
	v_fma_mixlo_f16 v171, v171, s51, 0
	ds_bpermute_b32 v188, v172, v171
	ds_bpermute_b32 v189, v173, v171
	ds_bpermute_b32 v190, v174, v171
	ds_bpermute_b32 v191, v175, v171
	ds_bpermute_b32 v192, v176, v171
	ds_bpermute_b32 v193, v177, v171
	ds_bpermute_b32 v194, v178, v171
	ds_bpermute_b32 v195, v179, v171
	v_mov_b32_e32 v229, 0x44800000
	v_fma_mixlo_f16 v228, s40, v229, 0
	v_cvt_f32_f16_e32 v228, v228
	v_cvt_f64_f32_e32 v[212:213], v228
	v_add_f64 v[212:213], v[212:213], 0
	v_fma_mixlo_f16 v228, s41, v229, 0
	v_cvt_f32_f16_e32 v228, v228
	v_cvt_f64_f32_e32 v[214:215], v228
	v_add_f64 v[212:213], v[212:213], v[214:215]
	v_fma_mixlo_f16 v228, s42, v229, 0
	v_cvt_f32_f16_e32 v228, v228
	v_cvt_f64_f32_e32 v[214:215], v228
	v_add_f64 v[212:213], v[212:213], v[214:215]
	v_fma_mixlo_f16 v228, s43, v229, 0
	v_cvt_f32_f16_e32 v228, v228
	v_cvt_f64_f32_e32 v[214:215], v228
	v_add_f64 v[212:213], v[212:213], v[214:215]
	v_fma_mixlo_f16 v228, s44, v229, 0
	v_cvt_f32_f16_e32 v228, v228
	v_cvt_f64_f32_e32 v[214:215], v228
	v_add_f64 v[212:213], v[212:213], v[214:215]
	v_fma_mixlo_f16 v228, s45, v229, 0
	v_cvt_f32_f16_e32 v228, v228
	v_cvt_f64_f32_e32 v[214:215], v228
	v_add_f64 v[212:213], v[212:213], v[214:215]
	v_fma_mixlo_f16 v228, s46, v229, 0
	v_cvt_f32_f16_e32 v228, v228
	v_cvt_f64_f32_e32 v[214:215], v228
	v_add_f64 v[212:213], v[212:213], v[214:215]
	v_fma_mixlo_f16 v228, s47, v229, 0
	v_cvt_f32_f16_e32 v228, v228
	v_cvt_f64_f32_e32 v[214:215], v228
	v_add_f64 v[212:213], v[212:213], v[214:215]
	v_fma_mixlo_f16 v228, s48, v229, 0
	v_cvt_f32_f16_e32 v228, v228
	v_cvt_f64_f32_e32 v[214:215], v228
	v_add_f64 v[212:213], v[212:213], v[214:215]
	v_fma_mixlo_f16 v228, s49, v229, 0
	v_cvt_f32_f16_e32 v228, v228
	v_cvt_f64_f32_e32 v[214:215], v228
	v_add_f64 v[212:213], v[212:213], v[214:215]
	v_fma_mixlo_f16 v228, s50, v229, 0
	v_cvt_f32_f16_e32 v228, v228
	v_cvt_f64_f32_e32 v[214:215], v228
	v_add_f64 v[212:213], v[212:213], v[214:215]
	s_waitcnt lgkmcnt(7)
	ds_bpermute_b32 v196, v180, v171
	ds_bpermute_b32 v197, v181, v171
	ds_bpermute_b32 v198, v182, v171
	ds_bpermute_b32 v199, v183, v171
	ds_bpermute_b32 v200, v184, v171
	ds_bpermute_b32 v201, v185, v171
	ds_bpermute_b32 v202, v186, v171
	ds_bpermute_b32 v203, v187, v171
	v_mul_f64 v[212:213], v[212:213], v[212:213]
	v_mul_f64 v[216:217], v[212:213], 0.5
	v_add_f64 v[218:219], v[216:217], v[216:217]
	s_mov_b32 s36, 0xeb1c432d
	s_mov_b32 s37, 0x3f1a36e2
	v_mul_f64 v[220:221], v[212:213], s[36:37]
	v_mul_f64 v[222:223], v[216:217], v[218:219]
	v_fmac_f64_e32 v[222:223], v[212:213], v[220:221]
	v_add_f64 v[224:225], v[212:213], v[212:213]
	s_mov_b32 s36, 0x487fcb92
	s_mov_b32 s37, 0x3f4d7dbf
	v_mul_f64 v[226:227], v[212:213], s[36:37]
	v_cvt_f32_f64_e32 v0, v[226:227]
	v_mov_b32_e32 v1, v0
	v_mov_b32_e32 v2, v0
	v_mov_b32_e32 v3, v0
	v_cvt_f32_f64_e32 v10, v[218:219]
	v_cvt_f32_f64_e32 v11, v[222:223]
	v_cvt_f32_f64_e32 v12, v[212:213]
	v_cvt_f32_f64_e32 v13, v[224:225]
	v_mul_f64 v[226:227], v[212:213], v[226:227]
	v_cvt_f32_f64_e32 v14, v[226:227]
	v_lshlrev_b32_e32 v167, 2, v164
	s_cmp_eq_u32 s12, 0
	s_cselect_b32 s23, 6, 64
	v_add_u32_e32 v168, 0, v167
	v_cmp_gt_u32_e32 vcc, s23, v168
	s_nop 1
	v_cndmask_b32_e64 v15, 0, 1.0, vcc
	v_add_u32_e32 v168, 1, v167
	v_cmp_gt_u32_e32 vcc, s23, v168
	s_nop 1
	v_cndmask_b32_e64 v16, 0, 1.0, vcc
	v_add_u32_e32 v168, 2, v167
	v_cmp_gt_u32_e32 vcc, s23, v168
	s_nop 1
	v_cndmask_b32_e64 v17, 0, 1.0, vcc
	v_add_u32_e32 v168, 3, v167
	v_cmp_gt_u32_e32 vcc, s23, v168
	s_nop 1
	v_cndmask_b32_e64 v18, 0, 1.0, vcc
	v_and_b32_e32 v167, 31, v8
	v_lshlrev_b32_e32 v167, 4, v167
	s_lshl_b32 s24, s12, 11
	s_add_i32 s25, s12, 7
	s_and_b32 s25, s25, 7
	s_lshl_b32 s26, s25, 11
	v_or_b32_e32 v4, s24, v167
	v_or_b32_e32 v5, s26, v167
	s_lshl_b32 s28, s25, 2
	s_add_u32 s28, s28, 0x10000
	v_mov_b32_e32 v7, s28
	v_mov_b32_e32 v19, 0
	v_mov_b32_e32 v20, 0
	v_mov_b32_e32 v21, 0
	v_mov_b32_e32 v22, 0
	s_waitcnt lgkmcnt(0)
	v_cmp_lt_u32_e64 s[32:33], 31, v8
	v_cmp_gt_u32_e64 s[34:35], 32, v8
	v_pack_b32_f16 v24, v188, v189
	v_pack_b32_f16 v25, v190, v191
	v_pack_b32_f16 v26, v192, v193
	v_pack_b32_f16 v27, v194, v195
	v_pack_b32_f16 v167, v196, v197
	v_cndmask_b32_e64 v28, 0, v167, s[32:33]
	v_cndmask_b32_e64 v32, 0, v167, s[34:35]
	v_pack_b32_f16 v167, v198, v199
	v_cndmask_b32_e64 v29, 0, v167, s[32:33]
	v_cndmask_b32_e64 v33, 0, v167, s[34:35]
	v_pack_b32_f16 v167, v200, v201
	v_cndmask_b32_e64 v30, 0, v167, s[32:33]
	v_cndmask_b32_e64 v34, 0, v167, s[34:35]
	v_pack_b32_f16 v167, v202, v203
	v_cndmask_b32_e64 v31, 0, v167, s[32:33]
	v_cndmask_b32_e64 v35, 0, v167, s[34:35]
	s_waitcnt lgkmcnt(0)
	s_barrier
	s_cmp_lt_u32 s12, 4
	s_cbranch_scc1 .Lq_noprio
	s_setprio 3
